# fastentry
# speedup vs baseline: 1.0056x; 1.0056x over previous
_Z11prep_kernelPKfS0_S0_S0_S0_S0_S0_S0_PhPf:
	s_load_dwordx2 s[6:7], s[0:1], 0x40
	s_load_dwordx2 s[8:9], s[0:1], 0x8
	s_cmpk_ge_u32 s2, 0x216
	s_cbranch_scc1 .Lcomp_fast
	s_cmp_gt_u32 s2, 21
	s_mov_b64 s[4:5], -1
	s_cbranch_scc0 .LBB0_43
	s_cmpk_lt_u32 s2, 0x216
	s_cbranch_scc0 .LBB0_23
	v_and_b32_e32 v1, 0x7f, v0
	v_mov_b32_e32 v3, 0
	v_lshlrev_b32_e32 v2, 2, v1
	s_waitcnt lgkmcnt(0)
	v_lshl_add_u64 v[4:5], s[8:9], 0, v[2:3]
	v_add_co_u32_e32 v6, vcc, 0x3000, v4
	v_lshlrev_b32_e32 v1, 2, v0
	s_nop 0
	v_addc_co_u32_e32 v7, vcc, 0, v5, vcc
	v_add_co_u32_e32 v8, vcc, 0x2c000, v4
	v_or_b32_e32 v3, 0x2ce00, v1
	s_nop 0
	v_addc_co_u32_e32 v9, vcc, 0, v5, vcc
	global_load_dword v41, v[6:7], off offset:1536
	global_load_dword v39, v[6:7], off offset:2048
	global_load_dword v37, v[6:7], off offset:2560
	global_load_dword v36, v[8:9], off offset:1024
	global_load_dword v35, v[8:9], off offset:1536
	global_load_dword v34, v[8:9], off offset:2048
	global_load_dword v33, v[8:9], off offset:2560
	global_load_dword v32, v[8:9], off offset:3072
	v_add_co_u32_e32 v6, vcc, 0x2d000, v4
	s_load_dwordx2 s[4:5], s[0:1], 0x10
	s_nop 0
	v_addc_co_u32_e32 v7, vcc, 0, v5, vcc
	global_load_dword v42, v3, s[8:9]
	global_load_dword v44, v[6:7], off
	global_load_dword v43, v[6:7], off offset:512
	global_load_dword v40, v[6:7], off offset:1024
	global_load_dword v38, v[6:7], off offset:1536
	global_load_dword v26, v[6:7], off offset:2048
	global_load_dword v27, v[6:7], off offset:2560
	global_load_dword v28, v[6:7], off offset:3072
	v_add_co_u32_e32 v6, vcc, 0x2e000, v4
	v_or_b32_e32 v3, 0x2de00, v1
	s_nop 0
	v_addc_co_u32_e32 v7, vcc, 0, v5, vcc
	global_load_dword v24, v3, s[8:9]
	global_load_dword v29, v[6:7], off
	global_load_dword v30, v[6:7], off offset:512
	global_load_dword v31, v[6:7], off offset:1024
	global_load_dword v25, v[6:7], off offset:1536
	global_load_dword v18, v[6:7], off offset:2048
	global_load_dword v19, v[6:7], off offset:2560
	global_load_dword v20, v[6:7], off offset:3072
	v_add_co_u32_e32 v6, vcc, 0x2f000, v4
	v_or_b32_e32 v3, 0x2ee00, v1
	s_nop 0
	v_addc_co_u32_e32 v7, vcc, 0, v5, vcc
	global_load_dword v16, v3, s[8:9]
	global_load_dword v21, v[6:7], off
	global_load_dword v22, v[6:7], off offset:512
	global_load_dword v23, v[6:7], off offset:1024
	global_load_dword v17, v[6:7], off offset:1536
	global_load_dword v10, v[6:7], off offset:2048
	global_load_dword v11, v[6:7], off offset:2560
	global_load_dword v12, v[6:7], off offset:3072
	v_or_b32_e32 v3, 0x2fe00, v1
	v_add_co_u32_e32 v4, vcc, 0x30000, v4
	s_lshl_b32 s3, s2, 3
	s_nop 0
	v_addc_co_u32_e32 v5, vcc, 0, v5, vcc
	global_load_dword v7, v3, s[8:9]
	global_load_dword v13, v[4:5], off
	global_load_dword v14, v[4:5], off offset:512
	global_load_dword v15, v[4:5], off offset:1024
	global_load_dword v9, v[4:5], off offset:1536
	global_load_dword v8, v[4:5], off offset:2048
	global_load_dword v6, v[4:5], off offset:2560
	s_waitcnt lgkmcnt(0)
	global_load_dword v1, v2, s[4:5]
	s_load_dwordx2 s[4:5], s[0:1], 0x0
	s_addk_i32 s3, 0xff50
	v_or_b32_e32 v3, 0x100, v0
	v_mul_u32_u24_e32 v46, 0x691, v0
	v_mul_u32_u24_e32 v55, 0x691, v3
	v_lshrrev_b32_e32 v46, 16, v46
	v_lshrrev_b32_e32 v55, 16, v55
	v_mul_u32_u24_e32 v4, 39, v46
	v_mul_u32_u24_e32 v5, 39, v55
	v_sub_u32_e32 v45, v0, v4
	v_sub_u32_e32 v54, v3, v5
	v_cmp_gt_u32_e32 vcc, 21, v45
	v_add_u32_e32 v4, -3, v45
	v_add_u32_e32 v5, -21, v45
	s_mov_b64 s[12:13], vcc
	v_cndmask_b32_e32 v47, v5, v4, vcc
	v_cmp_gt_u32_e32 vcc, 3, v45
	v_mul_u32_u24_e32 v48, 43, v47
	v_lshrrev_b32_e32 v48, 8, v48
	s_mov_b64 s[14:15], vcc
	v_mul_u32_u24_e32 v4, 6, v48
	v_sub_u32_e32 v49, v47, v4
	v_cndmask_b32_e32 v48, v48, v45, vcc
	v_add_u32_e32 v50, s3, v46
	v_lshl_add_u32 v50, v50, 1, v50
	v_add_u32_e32 v50, v50, v48
	v_lshlrev_b32_e32 v50, 2, v50
	v_lshlrev_b32_e64 v51, v49, 1
	v_cvt_f32_u32_e32 v51, v51
	v_mul_f32_e32 v51, 0.15915494, v51
	v_lshlrev_b32_e32 v53, 2, v46
	v_lshl_add_u32 v53, v45, 5, v53
	v_cmp_gt_u32_e32 vcc, 21, v54
	v_add_u32_e32 v4, -3, v54
	v_add_u32_e32 v5, -21, v54
	s_mov_b64 s[16:17], vcc
	v_cndmask_b32_e32 v56, v5, v4, vcc
	v_cmp_gt_u32_e32 vcc, 3, v54
	v_mul_u32_u24_e32 v57, 43, v56
	v_lshrrev_b32_e32 v57, 8, v57
	s_mov_b64 s[18:19], vcc
	v_mul_u32_u24_e32 v4, 6, v57
	v_sub_u32_e32 v58, v56, v4
	v_cndmask_b32_e32 v57, v57, v54, vcc
	v_add_u32_e32 v59, s3, v55
	v_lshl_add_u32 v59, v59, 1, v59
	v_add_u32_e32 v59, v59, v57
	v_lshlrev_b32_e32 v59, 2, v59
	v_lshlrev_b32_e64 v60, v58, 1
	v_cvt_f32_u32_e32 v60, v60
	v_mul_f32_e32 v60, 0.15915494, v60
	v_lshlrev_b32_e32 v62, 2, v55
	v_lshl_add_u32 v62, v54, 5, v62
	s_waitcnt lgkmcnt(0)
	global_load_dword v52, v50, s[4:5]
	v_cmp_gt_u32_e32 vcc, 56, v0
	s_and_saveexec_b64 s[10:11], vcc
	s_cbranch_execz .Lenc_skip1
	global_load_dword v61, v59, s[4:5]

.Lcomp_fast:
	s_load_dwordx4 s[12:15], s[0:1], 0x28
	s_load_dwordx2 s[4:5], s[0:1], 0x38
	s_load_dwordx2 s[24:25], s[0:1], 0x48
	s_lshl_b32 s3, s2, 2
	s_addk_i32 s3, 0xf7a8
	v_lshrrev_b32_e32 v1, 6, v0
	v_or_b32_e32 v2, s3, v1
	v_ashrrev_i32_e32 v3, 31, v2
	v_and_b32_e32 v7, 63, v0
	v_lshlrev_b64 v[4:5], 7, v[2:3]
	v_or_b32_e32 v4, v4, v7
	v_lshlrev_b64 v[12:13], 2, v[4:5]
	s_waitcnt lgkmcnt(0)
	v_lshl_add_u64 v[8:9], s[12:13], 0, v[12:13]
	global_load_dword v10, v[8:9], off nt
	global_load_dword v11, v[8:9], off offset:256 nt
	v_lshl_add_u64 v[14:15], s[14:15], 0, v[12:13]
	v_lshl_add_u64 v[12:13], s[4:5], 0, v[12:13]
	global_load_dword v9, v[14:15], off nt
	global_load_dword v8, v[14:15], off offset:256 nt
	global_load_dword v1, v[12:13], off nt
	global_load_dword v6, v[12:13], off offset:256 nt
	s_mov_b32 s3, 0xbfb8aa3b
	s_waitcnt vmcnt(5)
	v_add_f32_e32 v10, 0xc1200000, v10
	v_mul_f32_e64 v12, |v10|, s3
	v_exp_f32_e32 v13, v12
	s_mov_b32 s3, 0x3c23d70a
	v_cmp_ngt_f32_e32 vcc, s3, v13
	s_and_saveexec_b64 s[4:5], vcc
	s_xor_b64 s[10:11], exec, s[4:5]
	s_cbranch_execz .LBB0_26
	v_add_f32_e32 v12, 1.0, v13
	s_mov_b32 s3, 0x800000
	v_cmp_gt_f32_e32 vcc, s3, v12
	s_mov_b32 s3, 0x3f317217
	s_nop 0
	v_cndmask_b32_e64 v13, 0, 32, vcc
	v_ldexp_f32 v12, v12, v13
	v_log_f32_e32 v12, v12
	s_nop 0
	v_mul_f32_e32 v13, 0x3f317217, v12
	v_fma_f32 v13, v12, s3, -v13
	v_fmamk_f32 v13, v12, 0x3377d1cf, v13
	s_mov_b32 s3, 0x7f800000
	v_fmac_f32_e32 v13, 0x3f317217, v12
	v_cmp_lt_f32_e64 s[4:5], |v12|, s3
	s_nop 1
	v_cndmask_b32_e64 v12, v12, v13, s[4:5]
	v_mov_b32_e32 v13, 0x41b17218
	v_cndmask_b32_e32 v13, 0, v13, vcc
	v_sub_f32_e32 v12, v12, v13
